# E3p: E2 + NSA sel/win epilogue A2 read-modify-write loads hoisted (16 loads up front), nop-padded to keep code addresses
# speedup vs baseline: 1.0001x; 1.0001x over previous
.LBB0_518:
	v_mov_b32_e32 v0, v4
	s_nop 1
	v_permlane16_swap_b32_e32 v4, v0
	v_or_b32_e32 v71, 64, v132
	s_waitcnt vmcnt(0)
	global_load_dwordx2 v[198:199], v[130:131], off
	global_load_dwordx2 v[200:201], v[130:131], off offset:32
	global_load_dwordx2 v[202:203], v[130:131], off offset:64
	global_load_dwordx2 v[204:205], v[130:131], off offset:96
	global_load_dwordx2 v[206:207], v[130:131], off offset:128
	global_load_dwordx2 v[208:209], v[130:131], off offset:160
	global_load_dwordx2 v[210:211], v[130:131], off offset:192
	global_load_dwordx2 v[212:213], v[130:131], off offset:224
	v_or_b32_e32 v214, v71, v164
	global_load_ushort v214, v214, s[26:27]
	global_load_dwordx2 v[216:217], v[128:129], off
	global_load_dwordx2 v[218:219], v[128:129], off offset:32
	global_load_dwordx2 v[220:221], v[128:129], off offset:64
	global_load_dwordx2 v[222:223], v[128:129], off offset:96
	global_load_dwordx2 v[224:225], v[128:129], off offset:128
	global_load_dwordx2 v[228:229], v[128:129], off offset:160
	global_load_dwordx2 v[230:231], v[128:129], off offset:192
	global_load_dwordx2 v[232:233], v[128:129], off offset:224
	v_add_f32_e32 v5, v4, v0
	v_or_b32_e32 v0, v71, v163
	global_load_ushort v0, v0, s[26:27]
	v_mov_b32_e32 v125, v5
	s_nop 1
	v_permlane32_swap_b32_e32 v5, v125
	s_mov_b32 s8, 1
	s_waitcnt vmcnt(0)
	v_lshlrev_b32_e32 v0, 16, v0
	v_mul_f32_e32 v0, 0xbfb8aa3b, v0
	v_exp_f32_e32 v4, v0
	s_nop 0
	v_pk_add_f32 v[4:5], v[4:5], v[124:125]
	s_nop 0
	v_div_scale_f32 v0, s[0:1], v4, v4, 1.0
	v_rcp_f32_e32 v2, v0
	s_nop 0
	v_fma_f32 v72, -v0, v2, 1.0
	v_fmac_f32_e32 v2, v72, v2
	v_div_scale_f32 v72, vcc, 1.0, v4, 1.0
	v_mul_f32_e32 v73, v72, v2
	v_fma_f32 v74, -v0, v73, v72
	v_fmac_f32_e32 v73, v74, v2
	v_fma_f32 v0, -v0, v73, v72
	v_div_fmas_f32 v0, v0, v2, v73
	v_div_fixup_f32 v0, v0, v4, 1.0
	v_div_scale_f32 v2, s[0:1], v5, v5, v0
	v_rcp_f32_e32 v4, v2
	s_nop 0
	v_fma_f32 v72, -v2, v4, 1.0
	v_fmac_f32_e32 v4, v72, v4
	v_div_scale_f32 v72, vcc, v0, v5, v0
	v_mul_f32_e32 v73, v72, v4
	v_fma_f32 v74, -v2, v73, v72
	v_fmac_f32_e32 v73, v74, v4
	v_fma_f32 v2, -v2, v73, v72
	v_div_fmas_f32 v2, v2, v4, v73
	v_div_fixup_f32 v2, v2, v5, v0
	v_mov_b32_e32 v0, v70
	s_nop 1
	v_permlane16_swap_b32_e32 v70, v0
	v_lshlrev_b32_e32 v72, 16, v198
	v_and_b32_e32 v73, 0xffff0000, v198
	v_pk_fma_f32 v[66:67], v[66:67], v[2:3], v[72:73] op_sel_hi:[1,0,1]
	v_lshlrev_b32_e32 v4, 16, v199
	v_and_b32_e32 v5, 0xffff0000, v199
	v_pk_fma_f32 v[4:5], v[68:69], v[2:3], v[4:5] op_sel_hi:[1,0,1]
	v_cvt_pk_bf16_f32 v68, v66, v67
	v_cvt_pk_bf16_f32 v69, v4, v5
	global_store_dwordx2 v[130:131], v[68:69], off
	v_lshlrev_b32_e32 v68, 16, v200
	v_and_b32_e32 v69, 0xffff0000, v200
	v_pk_fma_f32 v[68:69], v[62:63], v[2:3], v[68:69] op_sel_hi:[1,0,1]
	v_lshlrev_b32_e32 v62, 16, v201
	v_and_b32_e32 v63, 0xffff0000, v201
	v_pk_fma_f32 v[62:63], v[64:65], v[2:3], v[62:63] op_sel_hi:[1,0,1]
	v_cvt_pk_bf16_f32 v64, v68, v69
	v_cvt_pk_bf16_f32 v65, v62, v63
	global_store_dwordx2 v[130:131], v[64:65], off offset:32
	v_lshlrev_b32_e32 v64, 16, v202
	v_and_b32_e32 v65, 0xffff0000, v202
	v_pk_fma_f32 v[64:65], v[58:59], v[2:3], v[64:65] op_sel_hi:[1,0,1]
	v_lshlrev_b32_e32 v58, 16, v203
	v_and_b32_e32 v59, 0xffff0000, v203
	v_pk_fma_f32 v[58:59], v[60:61], v[2:3], v[58:59] op_sel_hi:[1,0,1]
	v_cvt_pk_bf16_f32 v60, v64, v65
	v_cvt_pk_bf16_f32 v61, v58, v59
	global_store_dwordx2 v[130:131], v[60:61], off offset:64
	v_lshlrev_b32_e32 v60, 16, v204
	v_and_b32_e32 v61, 0xffff0000, v204
	v_pk_fma_f32 v[60:61], v[54:55], v[2:3], v[60:61] op_sel_hi:[1,0,1]
	v_lshlrev_b32_e32 v54, 16, v205
	v_and_b32_e32 v55, 0xffff0000, v205
	v_pk_fma_f32 v[54:55], v[56:57], v[2:3], v[54:55] op_sel_hi:[1,0,1]
	v_cvt_pk_bf16_f32 v56, v60, v61
	v_cvt_pk_bf16_f32 v57, v54, v55
	global_store_dwordx2 v[130:131], v[56:57], off offset:96
	v_lshlrev_b32_e32 v56, 16, v206
	v_and_b32_e32 v57, 0xffff0000, v206
	v_pk_fma_f32 v[56:57], v[50:51], v[2:3], v[56:57] op_sel_hi:[1,0,1]
	v_lshlrev_b32_e32 v50, 16, v207
	v_and_b32_e32 v51, 0xffff0000, v207
	v_pk_fma_f32 v[50:51], v[52:53], v[2:3], v[50:51] op_sel_hi:[1,0,1]
	v_cvt_pk_bf16_f32 v52, v56, v57
	v_cvt_pk_bf16_f32 v53, v50, v51
	global_store_dwordx2 v[130:131], v[52:53], off offset:128
	v_lshlrev_b32_e32 v52, 16, v208
	v_and_b32_e32 v53, 0xffff0000, v208
	v_pk_fma_f32 v[52:53], v[46:47], v[2:3], v[52:53] op_sel_hi:[1,0,1]
	v_lshlrev_b32_e32 v46, 16, v209
	v_and_b32_e32 v47, 0xffff0000, v209
	v_pk_fma_f32 v[46:47], v[48:49], v[2:3], v[46:47] op_sel_hi:[1,0,1]
	v_cvt_pk_bf16_f32 v48, v52, v53
	v_cvt_pk_bf16_f32 v49, v46, v47
	global_store_dwordx2 v[130:131], v[48:49], off offset:160
	v_lshlrev_b32_e32 v48, 16, v210
	v_and_b32_e32 v49, 0xffff0000, v210
	v_pk_fma_f32 v[48:49], v[42:43], v[2:3], v[48:49] op_sel_hi:[1,0,1]
	v_lshlrev_b32_e32 v42, 16, v211
	v_and_b32_e32 v43, 0xffff0000, v211
	v_pk_fma_f32 v[42:43], v[44:45], v[2:3], v[42:43] op_sel_hi:[1,0,1]
	v_cvt_pk_bf16_f32 v44, v48, v49
	v_cvt_pk_bf16_f32 v45, v42, v43
	global_store_dwordx2 v[130:131], v[44:45], off offset:192
	v_lshlrev_b32_e32 v72, 16, v212
	v_and_b32_e32 v73, 0xffff0000, v212
	v_lshlrev_b32_e32 v44, 16, v213
	v_and_b32_e32 v45, 0xffff0000, v213
	v_pk_fma_f32 v[38:39], v[38:39], v[2:3], v[72:73] op_sel_hi:[1,0,1]
	v_pk_fma_f32 v[40:41], v[40:41], v[2:3], v[44:45] op_sel_hi:[1,0,1]
	v_cvt_pk_bf16_f32 v44, v38, v39
	v_cvt_pk_bf16_f32 v45, v40, v41
	global_store_dwordx2 v[130:131], v[44:45], off offset:224
	v_add_f32_e32 v45, v70, v0
	v_mov_b32_e32 v125, v45
	s_nop 1
	v_permlane32_swap_b32_e32 v45, v125
	v_lshlrev_b32_e32 v0, 16, v214
	v_mul_f32_e32 v0, 0xbfb8aa3b, v0
	v_exp_f32_e32 v44, v0
	s_nop 0
	v_pk_add_f32 v[44:45], v[44:45], v[124:125]
	s_nop 0
	v_div_scale_f32 v0, s[0:1], v44, v44, 1.0
	v_rcp_f32_e32 v2, v0
	s_nop 0
	v_fma_f32 v70, -v0, v2, 1.0
	v_fmac_f32_e32 v2, v70, v2
	v_div_scale_f32 v70, vcc, 1.0, v44, 1.0
	v_mul_f32_e32 v71, v70, v2
	v_fma_f32 v72, -v0, v71, v70
	v_fmac_f32_e32 v71, v72, v2
	v_fma_f32 v0, -v0, v71, v70
	v_div_fmas_f32 v0, v0, v2, v71
	v_div_fixup_f32 v0, v0, v44, 1.0
	v_div_scale_f32 v2, s[0:1], v45, v45, v0
	v_rcp_f32_e32 v44, v2
	s_mov_b64 s[0:1], 0
	v_fma_f32 v70, -v2, v44, 1.0
	v_fmac_f32_e32 v44, v70, v44
	v_div_scale_f32 v70, vcc, v0, v45, v0
	v_mul_f32_e32 v71, v70, v44
	v_fma_f32 v72, -v2, v71, v70
	v_fmac_f32_e32 v71, v72, v44
	v_fma_f32 v2, -v2, v71, v70
	v_div_fmas_f32 v2, v2, v44, v71
	v_div_fixup_f32 v2, v2, v45, v0
	s_and_b64 vcc, exec, s[20:21]
	v_lshlrev_b32_e32 v44, 16, v216
	v_and_b32_e32 v45, 0xffff0000, v216
	v_pk_fma_f32 v[44:45], v[34:35], v[2:3], v[44:45] op_sel_hi:[1,0,1]
	v_lshlrev_b32_e32 v34, 16, v217
	v_and_b32_e32 v35, 0xffff0000, v217
	v_pk_fma_f32 v[34:35], v[36:37], v[2:3], v[34:35] op_sel_hi:[1,0,1]
	v_cvt_pk_bf16_f32 v36, v44, v45
	v_cvt_pk_bf16_f32 v37, v34, v35
	global_store_dwordx2 v[128:129], v[36:37], off
	v_lshlrev_b32_e32 v36, 16, v218
	v_and_b32_e32 v37, 0xffff0000, v218
	v_pk_fma_f32 v[36:37], v[30:31], v[2:3], v[36:37] op_sel_hi:[1,0,1]
	v_lshlrev_b32_e32 v30, 16, v219
	v_and_b32_e32 v31, 0xffff0000, v219
	v_pk_fma_f32 v[30:31], v[32:33], v[2:3], v[30:31] op_sel_hi:[1,0,1]
	v_cvt_pk_bf16_f32 v32, v36, v37
	v_cvt_pk_bf16_f32 v33, v30, v31
	global_store_dwordx2 v[128:129], v[32:33], off offset:32
	v_lshlrev_b32_e32 v32, 16, v220
	v_and_b32_e32 v33, 0xffff0000, v220
	v_pk_fma_f32 v[32:33], v[26:27], v[2:3], v[32:33] op_sel_hi:[1,0,1]
	v_lshlrev_b32_e32 v26, 16, v221
	v_and_b32_e32 v27, 0xffff0000, v221
	v_pk_fma_f32 v[26:27], v[28:29], v[2:3], v[26:27] op_sel_hi:[1,0,1]
	v_cvt_pk_bf16_f32 v28, v32, v33
	v_cvt_pk_bf16_f32 v29, v26, v27
	global_store_dwordx2 v[128:129], v[28:29], off offset:64
	v_lshlrev_b32_e32 v28, 16, v222
	v_and_b32_e32 v29, 0xffff0000, v222
	v_pk_fma_f32 v[28:29], v[22:23], v[2:3], v[28:29] op_sel_hi:[1,0,1]
	v_lshlrev_b32_e32 v22, 16, v223
	v_and_b32_e32 v23, 0xffff0000, v223
	v_pk_fma_f32 v[22:23], v[24:25], v[2:3], v[22:23] op_sel_hi:[1,0,1]
	v_cvt_pk_bf16_f32 v24, v28, v29
	v_cvt_pk_bf16_f32 v25, v22, v23
	global_store_dwordx2 v[128:129], v[24:25], off offset:96
	v_lshlrev_b32_e32 v24, 16, v224
	v_and_b32_e32 v25, 0xffff0000, v224
	v_pk_fma_f32 v[24:25], v[18:19], v[2:3], v[24:25] op_sel_hi:[1,0,1]
	v_lshlrev_b32_e32 v18, 16, v225
	v_and_b32_e32 v19, 0xffff0000, v225
	v_pk_fma_f32 v[18:19], v[20:21], v[2:3], v[18:19] op_sel_hi:[1,0,1]
	v_cvt_pk_bf16_f32 v20, v24, v25
	v_cvt_pk_bf16_f32 v21, v18, v19
	global_store_dwordx2 v[128:129], v[20:21], off offset:128
	v_lshlrev_b32_e32 v20, 16, v228
	v_and_b32_e32 v21, 0xffff0000, v228
	v_pk_fma_f32 v[20:21], v[14:15], v[2:3], v[20:21] op_sel_hi:[1,0,1]
	v_lshlrev_b32_e32 v14, 16, v229
	v_and_b32_e32 v15, 0xffff0000, v229
	v_pk_fma_f32 v[14:15], v[16:17], v[2:3], v[14:15] op_sel_hi:[1,0,1]
	v_cvt_pk_bf16_f32 v16, v20, v21
	v_cvt_pk_bf16_f32 v17, v14, v15
	global_store_dwordx2 v[128:129], v[16:17], off offset:160
	v_lshlrev_b32_e32 v16, 16, v230
	v_and_b32_e32 v17, 0xffff0000, v230
	v_pk_fma_f32 v[16:17], v[10:11], v[2:3], v[16:17] op_sel_hi:[1,0,1]
	v_lshlrev_b32_e32 v10, 16, v231
	v_and_b32_e32 v11, 0xffff0000, v231
	v_pk_fma_f32 v[10:11], v[12:13], v[2:3], v[10:11] op_sel_hi:[1,0,1]
	v_cvt_pk_bf16_f32 v12, v16, v17
	v_cvt_pk_bf16_f32 v13, v10, v11
	global_store_dwordx2 v[128:129], v[12:13], off offset:192
	v_lshlrev_b32_e32 v70, 16, v232
	v_and_b32_e32 v71, 0xffff0000, v232
	v_lshlrev_b32_e32 v12, 16, v233
	v_and_b32_e32 v13, 0xffff0000, v233
	v_pk_fma_f32 v[8:9], v[8:9], v[2:3], v[12:13] op_sel_hi:[1,0,1]
	v_mov_b32_e32 v13, v44
	v_mov_b32_e32 v44, v67
	v_mov_b32_e32 v12, v66
	v_pk_mul_f32 v[44:45], v[44:45], v[44:45]
	v_pk_fma_f32 v[6:7], v[6:7], v[2:3], v[70:71] op_sel_hi:[1,0,1]
	v_pk_fma_f32 v[12:13], v[12:13], v[12:13], v[44:45]
	v_mov_b32_e32 v45, v34
	v_mov_b32_e32 v34, v5
	v_mov_b32_e32 v44, v4
	v_pk_mul_f32 v[4:5], v[34:35], v[34:35]
	s_nop 0
	v_pk_fma_f32 v[4:5], v[44:45], v[44:45], v[4:5]
	s_nop 0
	v_pk_add_f32 v[4:5], v[12:13], v[4:5]
	v_mov_b32_e32 v13, v36
	v_mov_b32_e32 v36, v69
	v_mov_b32_e32 v12, v68
	v_pk_mul_f32 v[34:35], v[36:37], v[36:37]
	v_pk_add_f32 v[4:5], v[126:127], v[4:5]
	v_pk_fma_f32 v[12:13], v[12:13], v[12:13], v[34:35]
	v_mov_b32_e32 v35, v30
	v_mov_b32_e32 v30, v63
	v_mov_b32_e32 v34, v62
	v_pk_mul_f32 v[30:31], v[30:31], v[30:31]
	s_nop 0
	v_pk_fma_f32 v[30:31], v[34:35], v[34:35], v[30:31]
	s_nop 0
	v_pk_add_f32 v[12:13], v[12:13], v[30:31]
	s_nop 0
	v_pk_add_f32 v[4:5], v[12:13], v[4:5]
	v_mov_b32_e32 v13, v32
	v_mov_b32_e32 v32, v65
	v_mov_b32_e32 v12, v64
	v_pk_mul_f32 v[30:31], v[32:33], v[32:33]
	s_nop 0
	v_pk_fma_f32 v[12:13], v[12:13], v[12:13], v[30:31]
	v_mov_b32_e32 v31, v26
	v_mov_b32_e32 v26, v59
	v_mov_b32_e32 v30, v58
	v_pk_mul_f32 v[26:27], v[26:27], v[26:27]
	s_nop 0
	v_pk_fma_f32 v[26:27], v[30:31], v[30:31], v[26:27]
	s_nop 0
	v_pk_add_f32 v[12:13], v[12:13], v[26:27]
	s_nop 0
	v_pk_add_f32 v[4:5], v[12:13], v[4:5]
	v_mov_b32_e32 v13, v28
	v_mov_b32_e32 v28, v61
	v_mov_b32_e32 v12, v60
	v_pk_mul_f32 v[26:27], v[28:29], v[28:29]
	s_nop 0
	v_pk_fma_f32 v[12:13], v[12:13], v[12:13], v[26:27]
	v_mov_b32_e32 v27, v22
	v_mov_b32_e32 v22, v55
	v_mov_b32_e32 v26, v54
	v_pk_mul_f32 v[22:23], v[22:23], v[22:23]
	s_nop 0
	v_pk_fma_f32 v[22:23], v[26:27], v[26:27], v[22:23]
	s_nop 0
	v_pk_add_f32 v[12:13], v[12:13], v[22:23]
	s_nop 0
	v_pk_add_f32 v[4:5], v[12:13], v[4:5]
	v_mov_b32_e32 v13, v24
	v_mov_b32_e32 v24, v57
	v_mov_b32_e32 v12, v56
	v_pk_mul_f32 v[22:23], v[24:25], v[24:25]
	s_nop 0
	v_pk_fma_f32 v[12:13], v[12:13], v[12:13], v[22:23]
	v_mov_b32_e32 v23, v18
	v_mov_b32_e32 v18, v51
	v_mov_b32_e32 v22, v50
	v_pk_mul_f32 v[18:19], v[18:19], v[18:19]
	s_nop 0
	v_pk_fma_f32 v[18:19], v[22:23], v[22:23], v[18:19]
	s_nop 0
	v_pk_add_f32 v[12:13], v[12:13], v[18:19]
	s_nop 0
	v_pk_add_f32 v[4:5], v[12:13], v[4:5]
	v_mov_b32_e32 v13, v20
	v_mov_b32_e32 v20, v53
	v_mov_b32_e32 v12, v52
	v_pk_mul_f32 v[18:19], v[20:21], v[20:21]
	s_nop 0
	v_pk_fma_f32 v[12:13], v[12:13], v[12:13], v[18:19]
	v_mov_b32_e32 v19, v14
	v_mov_b32_e32 v14, v47
	v_mov_b32_e32 v18, v46
	v_pk_mul_f32 v[14:15], v[14:15], v[14:15]
	s_nop 0
	v_pk_fma_f32 v[14:15], v[18:19], v[18:19], v[14:15]
	s_nop 0
	v_pk_add_f32 v[12:13], v[12:13], v[14:15]
	s_nop 0
	v_pk_add_f32 v[4:5], v[12:13], v[4:5]
	v_mov_b32_e32 v13, v16
	v_mov_b32_e32 v16, v49
	v_mov_b32_e32 v12, v48
	v_pk_mul_f32 v[14:15], v[16:17], v[16:17]
	s_nop 0
	v_pk_fma_f32 v[12:13], v[12:13], v[12:13], v[14:15]
	v_mov_b32_e32 v15, v10
	v_mov_b32_e32 v10, v43
	v_mov_b32_e32 v14, v42
	v_pk_mul_f32 v[10:11], v[10:11], v[10:11]
	s_nop 0
	v_pk_fma_f32 v[10:11], v[14:15], v[14:15], v[10:11]
	v_mov_b32_e32 v14, v41
	v_pk_add_f32 v[10:11], v[12:13], v[10:11]
	v_mov_b32_e32 v12, v39
	v_mov_b32_e32 v13, v7
	v_pk_add_f32 v[4:5], v[10:11], v[4:5]
	v_mov_b32_e32 v10, v38
	v_mov_b32_e32 v11, v6
	v_pk_mul_f32 v[12:13], v[12:13], v[12:13]
	v_mov_b32_e32 v15, v9
	v_pk_fma_f32 v[10:11], v[10:11], v[10:11], v[12:13]
	v_mov_b32_e32 v12, v40
	v_mov_b32_e32 v13, v8
	v_pk_mul_f32 v[14:15], v[14:15], v[14:15]
	s_nop 0
	v_pk_fma_f32 v[12:13], v[12:13], v[12:13], v[14:15]
	s_nop 0
	v_pk_add_f32 v[10:11], v[10:11], v[12:13]
	s_nop 0
	v_pk_add_f32 v[126:127], v[10:11], v[4:5]
	v_cvt_pk_bf16_f32 v4, v6, v7
	v_cvt_pk_bf16_f32 v5, v8, v9
	global_store_dwordx2 v[128:129], v[4:5], off offset:224
	s_cbranch_vccnz .LBB0_515
	s_nop 0
	s_nop 0
	s_nop 0
	s_nop 0
	s_nop 0
	s_nop 0
	s_nop 0
	s_nop 0
	s_nop 0
	s_nop 0
	s_nop 0
	s_nop 0
	s_nop 0
	s_nop 0
	s_nop 0
	s_nop 0
	s_nop 0

.LBB0_782:
	v_mov_b32_e32 v0, v4
	s_nop 1
	v_permlane16_swap_b32_e32 v4, v0
	v_or_b32_e32 v71, 48, v132
	s_waitcnt vmcnt(0)
	v_add_f32_e32 v5, v4, v0
	global_load_dwordx2 v[198:199], v[130:131], off
	global_load_dwordx2 v[200:201], v[130:131], off offset:32
	global_load_dwordx2 v[202:203], v[130:131], off offset:64
	global_load_dwordx2 v[204:205], v[130:131], off offset:96
	global_load_dwordx2 v[206:207], v[130:131], off offset:128
	global_load_dwordx2 v[208:209], v[130:131], off offset:160
	global_load_dwordx2 v[210:211], v[130:131], off offset:192
	global_load_dwordx2 v[212:213], v[130:131], off offset:224
	v_or_b32_e32 v214, v71, v164
	global_load_ushort v214, v214, s[26:27]
	global_load_dwordx2 v[216:217], v[128:129], off
	global_load_dwordx2 v[218:219], v[128:129], off offset:32
	global_load_dwordx2 v[220:221], v[128:129], off offset:64
	global_load_dwordx2 v[222:223], v[128:129], off offset:96
	global_load_dwordx2 v[224:225], v[128:129], off offset:128
	global_load_dwordx2 v[228:229], v[128:129], off offset:160
	global_load_dwordx2 v[230:231], v[128:129], off offset:192
	global_load_dwordx2 v[232:233], v[128:129], off offset:224
	v_or_b32_e32 v0, v71, v163
	global_load_ushort v0, v0, s[26:27]
	v_mov_b32_e32 v125, v5
	s_nop 1
	v_permlane32_swap_b32_e32 v5, v125
	s_mov_b32 s36, s90
	s_mov_b32 s33, s92
	s_waitcnt vmcnt(0)
	v_lshlrev_b32_e32 v0, 16, v0
	v_mul_f32_e32 v0, 0xbfb8aa3b, v0
	v_exp_f32_e32 v4, v0
	s_nop 0
	v_pk_add_f32 v[4:5], v[4:5], v[124:125]
	s_nop 0
	v_div_scale_f32 v0, s[0:1], v4, v4, 1.0
	v_rcp_f32_e32 v2, v0
	s_nop 0
	v_fma_f32 v72, -v0, v2, 1.0
	v_fmac_f32_e32 v2, v72, v2
	v_div_scale_f32 v72, vcc, 1.0, v4, 1.0
	v_mul_f32_e32 v73, v72, v2
	v_fma_f32 v74, -v0, v73, v72
	v_fmac_f32_e32 v73, v74, v2
	v_fma_f32 v0, -v0, v73, v72
	v_div_fmas_f32 v0, v0, v2, v73
	v_div_fixup_f32 v0, v0, v4, 1.0
	v_div_scale_f32 v2, s[0:1], v5, v5, v0
	v_rcp_f32_e32 v4, v2
	s_nop 0
	v_fma_f32 v72, -v2, v4, 1.0
	v_fmac_f32_e32 v4, v72, v4
	v_div_scale_f32 v72, vcc, v0, v5, v0
	v_mul_f32_e32 v73, v72, v4
	v_fma_f32 v74, -v2, v73, v72
	v_fmac_f32_e32 v73, v74, v4
	v_fma_f32 v2, -v2, v73, v72
	v_div_fmas_f32 v2, v2, v4, v73
	v_div_fixup_f32 v2, v2, v5, v0
	v_mov_b32_e32 v0, v70
	s_nop 1
	v_permlane16_swap_b32_e32 v70, v0
	v_lshlrev_b32_e32 v72, 16, v199
	v_and_b32_e32 v73, 0xffff0000, v199
	v_pk_fma_f32 v[68:69], v[68:69], v[2:3], v[72:73] op_sel_hi:[1,0,1]
	v_lshlrev_b32_e32 v72, 16, v198
	v_and_b32_e32 v73, 0xffff0000, v198
	v_pk_fma_f32 v[4:5], v[66:67], v[2:3], v[72:73] op_sel_hi:[1,0,1]
	s_nop 0
	v_cvt_pk_bf16_f32 v4, v4, v5
	v_cvt_pk_bf16_f32 v5, v68, v69
	global_store_dwordx2 v[130:131], v[4:5], off
	v_lshlrev_b32_e32 v66, 16, v201
	v_and_b32_e32 v67, 0xffff0000, v201
	v_pk_fma_f32 v[64:65], v[64:65], v[2:3], v[66:67] op_sel_hi:[1,0,1]
	v_lshlrev_b32_e32 v66, 16, v200
	v_and_b32_e32 v67, 0xffff0000, v200
	v_pk_fma_f32 v[4:5], v[62:63], v[2:3], v[66:67] op_sel_hi:[1,0,1]
	s_nop 0
	v_cvt_pk_bf16_f32 v4, v4, v5
	v_cvt_pk_bf16_f32 v5, v64, v65
	global_store_dwordx2 v[130:131], v[4:5], off offset:32
	v_lshlrev_b32_e32 v62, 16, v203
	v_and_b32_e32 v63, 0xffff0000, v203
	v_pk_fma_f32 v[60:61], v[60:61], v[2:3], v[62:63] op_sel_hi:[1,0,1]
	v_lshlrev_b32_e32 v62, 16, v202
	v_and_b32_e32 v63, 0xffff0000, v202
	v_pk_fma_f32 v[4:5], v[58:59], v[2:3], v[62:63] op_sel_hi:[1,0,1]
	s_nop 0
	v_cvt_pk_bf16_f32 v4, v4, v5
	v_cvt_pk_bf16_f32 v5, v60, v61
	global_store_dwordx2 v[130:131], v[4:5], off offset:64
	v_lshlrev_b32_e32 v58, 16, v205
	v_and_b32_e32 v59, 0xffff0000, v205
	v_pk_fma_f32 v[56:57], v[56:57], v[2:3], v[58:59] op_sel_hi:[1,0,1]
	v_lshlrev_b32_e32 v58, 16, v204
	v_and_b32_e32 v59, 0xffff0000, v204
	v_pk_fma_f32 v[4:5], v[54:55], v[2:3], v[58:59] op_sel_hi:[1,0,1]
	s_nop 0
	v_cvt_pk_bf16_f32 v4, v4, v5
	v_cvt_pk_bf16_f32 v5, v56, v57
	global_store_dwordx2 v[130:131], v[4:5], off offset:96
	v_lshlrev_b32_e32 v54, 16, v207
	v_and_b32_e32 v55, 0xffff0000, v207
	v_pk_fma_f32 v[52:53], v[52:53], v[2:3], v[54:55] op_sel_hi:[1,0,1]
	v_lshlrev_b32_e32 v54, 16, v206
	v_and_b32_e32 v55, 0xffff0000, v206
	v_pk_fma_f32 v[4:5], v[50:51], v[2:3], v[54:55] op_sel_hi:[1,0,1]
	s_nop 0
	v_cvt_pk_bf16_f32 v4, v4, v5
	v_cvt_pk_bf16_f32 v5, v52, v53
	global_store_dwordx2 v[130:131], v[4:5], off offset:128
	v_lshlrev_b32_e32 v50, 16, v209
	v_and_b32_e32 v51, 0xffff0000, v209
	v_pk_fma_f32 v[48:49], v[48:49], v[2:3], v[50:51] op_sel_hi:[1,0,1]
	v_lshlrev_b32_e32 v50, 16, v208
	v_and_b32_e32 v51, 0xffff0000, v208
	v_pk_fma_f32 v[4:5], v[46:47], v[2:3], v[50:51] op_sel_hi:[1,0,1]
	s_nop 0
	v_cvt_pk_bf16_f32 v4, v4, v5
	v_cvt_pk_bf16_f32 v5, v48, v49
	global_store_dwordx2 v[130:131], v[4:5], off offset:160
	v_lshlrev_b32_e32 v46, 16, v211
	v_and_b32_e32 v47, 0xffff0000, v211
	v_pk_fma_f32 v[44:45], v[44:45], v[2:3], v[46:47] op_sel_hi:[1,0,1]
	v_lshlrev_b32_e32 v46, 16, v210
	v_and_b32_e32 v47, 0xffff0000, v210
	v_pk_fma_f32 v[4:5], v[42:43], v[2:3], v[46:47] op_sel_hi:[1,0,1]
	s_nop 0
	v_cvt_pk_bf16_f32 v4, v4, v5
	v_cvt_pk_bf16_f32 v5, v44, v45
	global_store_dwordx2 v[130:131], v[4:5], off offset:192
	v_lshlrev_b32_e32 v42, 16, v213
	v_and_b32_e32 v43, 0xffff0000, v213
	v_pk_fma_f32 v[40:41], v[40:41], v[2:3], v[42:43] op_sel_hi:[1,0,1]
	v_lshlrev_b32_e32 v42, 16, v212
	v_and_b32_e32 v43, 0xffff0000, v212
	v_pk_fma_f32 v[4:5], v[38:39], v[2:3], v[42:43] op_sel_hi:[1,0,1]
	s_nop 0
	v_cvt_pk_bf16_f32 v4, v4, v5
	v_cvt_pk_bf16_f32 v5, v40, v41
	global_store_dwordx2 v[130:131], v[4:5], off offset:224
	v_add_f32_e32 v5, v70, v0
	v_mov_b32_e32 v125, v5
	s_nop 1
	v_permlane32_swap_b32_e32 v5, v125
	v_lshlrev_b32_e32 v0, 16, v214
	v_mul_f32_e32 v0, 0xbfb8aa3b, v0
	v_exp_f32_e32 v4, v0
	s_nop 0
	v_pk_add_f32 v[4:5], v[4:5], v[124:125]
	s_nop 0
	v_div_scale_f32 v0, s[0:1], v4, v4, 1.0
	v_rcp_f32_e32 v2, v0
	s_nop 0
	v_fma_f32 v38, -v0, v2, 1.0
	v_fmac_f32_e32 v2, v38, v2
	v_div_scale_f32 v38, vcc, 1.0, v4, 1.0
	v_mul_f32_e32 v39, v38, v2
	v_fma_f32 v40, -v0, v39, v38
	v_fmac_f32_e32 v39, v40, v2
	v_fma_f32 v0, -v0, v39, v38
	v_div_fmas_f32 v0, v0, v2, v39
	v_div_fixup_f32 v0, v0, v4, 1.0
	v_div_scale_f32 v2, s[0:1], v5, v5, v0
	v_rcp_f32_e32 v4, v2
	s_mov_b32 s0, s97
	s_mov_b32 s1, s92
	v_fma_f32 v38, -v2, v4, 1.0
	v_fmac_f32_e32 v4, v38, v4
	v_div_scale_f32 v38, vcc, v0, v5, v0
	v_mul_f32_e32 v39, v38, v4
	v_fma_f32 v40, -v2, v39, v38
	v_fmac_f32_e32 v39, v40, v4
	v_fma_f32 v2, -v2, v39, v38
	v_div_fmas_f32 v2, v2, v4, v39
	v_div_fixup_f32 v2, v2, v5, v0
	s_andn2_b64 vcc, exec, s[18:19]
	v_lshlrev_b32_e32 v38, 16, v217
	v_and_b32_e32 v39, 0xffff0000, v217
	v_pk_fma_f32 v[36:37], v[36:37], v[2:3], v[38:39] op_sel_hi:[1,0,1]
	v_lshlrev_b32_e32 v38, 16, v216
	v_and_b32_e32 v39, 0xffff0000, v216
	v_pk_fma_f32 v[4:5], v[34:35], v[2:3], v[38:39] op_sel_hi:[1,0,1]
	s_nop 0
	v_cvt_pk_bf16_f32 v4, v4, v5
	v_cvt_pk_bf16_f32 v5, v36, v37
	global_store_dwordx2 v[128:129], v[4:5], off
	v_lshlrev_b32_e32 v34, 16, v219
	v_and_b32_e32 v35, 0xffff0000, v219
	v_pk_fma_f32 v[32:33], v[32:33], v[2:3], v[34:35] op_sel_hi:[1,0,1]
	v_lshlrev_b32_e32 v34, 16, v218
	v_and_b32_e32 v35, 0xffff0000, v218
	v_pk_fma_f32 v[4:5], v[30:31], v[2:3], v[34:35] op_sel_hi:[1,0,1]
	s_nop 0
	v_cvt_pk_bf16_f32 v4, v4, v5
	v_cvt_pk_bf16_f32 v5, v32, v33
	global_store_dwordx2 v[128:129], v[4:5], off offset:32
	v_lshlrev_b32_e32 v30, 16, v221
	v_and_b32_e32 v31, 0xffff0000, v221
	v_pk_fma_f32 v[28:29], v[28:29], v[2:3], v[30:31] op_sel_hi:[1,0,1]
	v_lshlrev_b32_e32 v30, 16, v220
	v_and_b32_e32 v31, 0xffff0000, v220
	v_pk_fma_f32 v[4:5], v[26:27], v[2:3], v[30:31] op_sel_hi:[1,0,1]
	s_nop 0
	v_cvt_pk_bf16_f32 v4, v4, v5
	v_cvt_pk_bf16_f32 v5, v28, v29
	global_store_dwordx2 v[128:129], v[4:5], off offset:64
	v_lshlrev_b32_e32 v26, 16, v223
	v_and_b32_e32 v27, 0xffff0000, v223
	v_pk_fma_f32 v[24:25], v[24:25], v[2:3], v[26:27] op_sel_hi:[1,0,1]
	v_lshlrev_b32_e32 v26, 16, v222
	v_and_b32_e32 v27, 0xffff0000, v222
	v_pk_fma_f32 v[4:5], v[22:23], v[2:3], v[26:27] op_sel_hi:[1,0,1]
	s_nop 0
	v_cvt_pk_bf16_f32 v4, v4, v5
	v_cvt_pk_bf16_f32 v5, v24, v25
	global_store_dwordx2 v[128:129], v[4:5], off offset:96
	v_lshlrev_b32_e32 v22, 16, v225
	v_and_b32_e32 v23, 0xffff0000, v225
	v_pk_fma_f32 v[20:21], v[20:21], v[2:3], v[22:23] op_sel_hi:[1,0,1]
	v_lshlrev_b32_e32 v22, 16, v224
	v_and_b32_e32 v23, 0xffff0000, v224
	v_pk_fma_f32 v[4:5], v[18:19], v[2:3], v[22:23] op_sel_hi:[1,0,1]
	s_nop 0
	v_cvt_pk_bf16_f32 v4, v4, v5
	v_cvt_pk_bf16_f32 v5, v20, v21
	global_store_dwordx2 v[128:129], v[4:5], off offset:128
	v_lshlrev_b32_e32 v18, 16, v229
	v_and_b32_e32 v19, 0xffff0000, v229
	v_pk_fma_f32 v[16:17], v[16:17], v[2:3], v[18:19] op_sel_hi:[1,0,1]
	v_lshlrev_b32_e32 v18, 16, v228
	v_and_b32_e32 v19, 0xffff0000, v228
	v_pk_fma_f32 v[4:5], v[14:15], v[2:3], v[18:19] op_sel_hi:[1,0,1]
	s_nop 0
	v_cvt_pk_bf16_f32 v4, v4, v5
	v_cvt_pk_bf16_f32 v5, v16, v17
	global_store_dwordx2 v[128:129], v[4:5], off offset:160
	v_lshlrev_b32_e32 v14, 16, v231
	v_and_b32_e32 v15, 0xffff0000, v231
	v_pk_fma_f32 v[12:13], v[12:13], v[2:3], v[14:15] op_sel_hi:[1,0,1]
	v_lshlrev_b32_e32 v14, 16, v230
	v_and_b32_e32 v15, 0xffff0000, v230
	v_pk_fma_f32 v[4:5], v[10:11], v[2:3], v[14:15] op_sel_hi:[1,0,1]
	s_nop 0
	v_cvt_pk_bf16_f32 v4, v4, v5
	v_cvt_pk_bf16_f32 v5, v12, v13
	global_store_dwordx2 v[128:129], v[4:5], off offset:192
	v_lshlrev_b32_e32 v10, 16, v233
	v_and_b32_e32 v11, 0xffff0000, v233
	v_pk_fma_f32 v[8:9], v[8:9], v[2:3], v[10:11] op_sel_hi:[1,0,1]
	v_lshlrev_b32_e32 v10, 16, v232
	v_and_b32_e32 v11, 0xffff0000, v232
	v_pk_fma_f32 v[4:5], v[6:7], v[2:3], v[10:11] op_sel_hi:[1,0,1]
	s_nop 0
	v_cvt_pk_bf16_f32 v4, v4, v5
	v_cvt_pk_bf16_f32 v5, v8, v9
	global_store_dwordx2 v[128:129], v[4:5], off offset:224
	s_cbranch_vccnz .LBB0_784
	s_nop 0
	s_nop 0
	s_nop 0
	s_nop 0
	s_nop 0
	s_nop 0
	s_nop 0
	s_nop 0
	s_nop 0
	s_nop 0
	s_nop 0
	s_nop 0
	s_nop 0
	s_nop 0
	s_nop 0
	s_nop 0
	s_nop 0
